# each layer converts its own MoE weights inside its own attention phase (layer 0: 1536 items, layers 1-3: 1216 items) instead of layer 0 carrying two layers' worth
# speedup vs baseline: 1.0097x; 1.0016x over previous
.LBB0_789:
	s_or_b64 exec, exec, s[2:3]
	v_readlane_b32 s2, v253, 55
	s_waitcnt lgkmcnt(0)
	s_barrier
	v_mov_b32_e32 v0, s2
	v_readlane_b32 s2, v253, 54
	ds_read_b32 v0, v0
	s_nop 0
	v_mov_b32_e32 v1, s2
	ds_read_b32 v1, v1
	s_waitcnt lgkmcnt(0)
	s_barrier
	v_add_u32_e32 v201, 0x580, v0
	s_nop 0
	v_readfirstlane_b32 s100, v201
	v_readlane_b32 s101, v254, 38
	s_nop 3
	s_movk_i32 vcc_lo, 0x4c0
	s_movk_i32 vcc_hi, 0xbe0
	s_cmp_eq_u32 s101, 0
	s_cselect_b32 vcc_lo, 0x600, vcc_lo
	s_cselect_b32 vcc_hi, 0xc00, vcc_hi
	s_add_i32 vcc_lo, s100, vcc_lo
	s_max_u32 vcc_lo, vcc_lo, vcc_hi
	v_mov_b32_e32 v201, vcc_lo
	v_readfirstlane_b32 s30, v0
	v_cmp_ge_i32_e32 vcc, v1, v201
	v_readfirstlane_b32 s24, v1
	s_cbranch_vccnz .LBB0_931
	s_add_u32 s31, s4, 0x37b00000
	s_addc_u32 s34, s5, 0
	s_add_i32 s35, s30, 0x480
	s_add_u32 s44, s4, 0x61800000
	s_addc_u32 s45, s5, 0
	s_add_u32 s46, s4, 0x42c00000
	s_addc_u32 s47, s5, 0
	s_add_u32 s10, s4, 0x66d00000
	s_addc_u32 s11, s5, 0
	s_add_u32 s48, s4, 0x61640000
	s_movk_i32 s2, 0x100
	s_addc_u32 s49, s5, 0
	v_cmp_gt_i32_e64 s[38:39], s2, v199
	s_add_i32 s2, 0, 0x14800
	v_add_u32_e32 v214, s2, v200
	s_add_i32 s2, 0, 0x16800
	s_cmp_lg_u32 0, -1
	v_lshlrev_b32_e32 v3, 1, v199
	v_lshlrev_b32_e32 v211, 4, v199
	s_cselect_b32 s3, 0, 0
	v_lshlrev_b32_e32 v0, 3, v199
	v_lshlrev_b32_e32 v1, 10, v101
	v_lshlrev_b32_e32 v2, 4, v198
	v_and_b32_e32 v3, 32, v3
	v_and_b32_e32 v5, 0xc0, v211
	s_addk_i32 s3, 0x6000
	v_and_b32_e32 v210, 24, v0
	v_lshl_or_b32 v5, v101, 8, v5
	v_add3_u32 v213, 0, v1, v2
	v_add_u32_e32 v1, s3, v3
	v_add3_u32 v217, v1, v210, v5
	v_lshrrev_b32_e32 v1, 3, v100
	v_lshl_add_u32 v215, v198, 2, s2
	v_and_b32_e32 v218, 56, v0
	v_lshl_add_u32 v220, v1, 2, s2
	s_add_i32 s2, 0, 0x14a00
	v_add_u32_e32 v4, 0, v3
	v_lshlrev_b32_e32 v96, 1, v218
	v_add_u32_e32 v221, s2, v200
	s_add_i32 s2, 0, 0x14900
	v_ashrrev_i32_e32 v203, 31, v202
	v_lshlrev_b32_e32 v208, 9, v100
	v_lshrrev_b32_e32 v209, 2, v100
	v_add3_u32 v212, v4, v210, v5
	v_cmp_gt_u32_e64 s[40:41], 32, v100
	v_cmp_lt_u32_e64 s[42:43], 31, v100
	v_or_b32_e32 v216, 0xc0, v206
	v_lshl_add_u64 v[204:205], s[4:5], 0, v[96:97]
	v_lshlrev_b32_e32 v219, 7, v1
	v_add_u32_e32 v222, s2, v200
	v_lshlrev_b32_e32 v96, 1, v98
	s_branch .LBB0_792

.LBB0_796:
	s_or_b64 exec, exec, s[2:3]
	v_readlane_b32 s101, v254, 38
	s_nop 3
	s_cmp_eq_u32 s101, 0
	s_cbranch_scc1 .Lc3_l0
	s_cmpk_lt_u32 s24, 0xbe0
	s_cbranch_scc0 .Lc3_late
	s_mul_hi_u32 s101, s24, 0xcccccccd
	s_lshr_b32 s101, s101, 2
	s_mul_i32 s2, s101, 5
	s_sub_i32 s2, s24, s2
	s_lshl_b32 s101, s101, 1
	s_cmp_eq_u32 s2, 1
	s_cbranch_scc1 .Lc3_entry
	s_cmp_eq_u32 s2, 3
	s_cbranch_scc0 .Lc3_r5a
	s_add_i32 s101, s101, 1
	s_branch .Lc3_entry

.Lc3_l0:
	s_cmpk_lt_u32 s24, 0xc00
	s_cbranch_scc0 .Lc3_late0
	s_lshr_b32 s101, s24, 1
	s_bitcmp1_b32 s24, 0
	s_cbranch_scc1 .Lc3_entry
	s_sub_i32 s24, s24, s101
	s_branch .Lc3_chk
.Lc3_late0:
	s_sub_i32 s24, s24, 0x600

.Lc3_entry:
	v_readlane_b32 s22, v252, 0
	v_readlane_b32 s23, v252, 1
	v_readlane_b32 s20, v254, 38
	s_lshr_b32 s2, s93, 6
	s_load_dwordx2 s[24:25], s[22:23], 0x98
	s_lshl_b32 s27, s2, 14
	v_mbcnt_lo_u32_b32 v169, -1, 0
	v_mbcnt_hi_u32_b32 v169, -1, v169
	s_cmp_lg_u32 s20, 0
	s_cbranch_scc1 .Lc3_nextl
	s_lshl_b32 s19, s101, 3
	s_add_i32 s19, s19, s2
	s_branch .Lc3_have
